# P3 main loop restructured to 4 phases per K-tile pair (16 MFMA per barrier interval, 8 barriers per iteration instead of 16), staging and counted waits re-derived
# baseline (speedup 1.0000x reference)
.LBB4_12:
	s_and_b32 s33, s0, 3
	s_add_u32 s12, s8, 0x80
	s_addc_u32 s0, s3, 0
	s_add_i32 s36, s7, 0x18000
	s_and_b32 s13, s0, 0xffff
	s_mov_b32 m0, s36
	s_add_i32 s37, s7, 0x1a000
	s_waitcnt vmcnt(4)
	s_barrier
	buffer_load_dwordx4 v193, s[12:15], 0 offen lds
	s_mov_b32 m0, s37
	v_lshrrev_b32_e32 v1, 4, v0
	buffer_load_dwordx4 v195, s[12:15], 0 offen lds
	s_add_u32 s12, s16, 0x80
	s_addc_u32 s0, s9, 0
	s_add_i32 s38, s7, 0x8000
	s_and_b32 s13, s0, 0xffff
	s_mov_b32 m0, s38
	s_add_i32 s39, s7, 0xa000
	buffer_load_dwordx4 v192, s[12:15], 0 offen lds
	s_mov_b32 m0, s39
	v_and_b32_e32 v196, 15, v0
	buffer_load_dwordx4 v194, s[12:15], 0 offen lds
	s_add_u32 s12, s8, 0x4080
	s_addc_u32 s0, s3, 0
	s_add_i32 s40, s7, 0x1c000
	s_and_b32 s13, s0, 0xffff
	s_mov_b32 m0, s40
	s_add_i32 s41, s7, 0x1e000
	buffer_load_dwordx4 v193, s[12:15], 0 offen lds
	s_mov_b32 m0, s41
	v_bfe_u32 v197, v0, 4, 2
	buffer_load_dwordx4 v195, s[12:15], 0 offen lds
	v_bfe_u32 v0, v0, 1, 3
	v_bitop3_b32 v0, v1, v0, 3 bitop3:0x6c
	v_lshlrev_b32_e32 v1, 7, v196
	v_lshlrev_b32_e32 v0, 4, v0
	v_lshl_or_b32 v2, s27, 13, v1
	v_lshl_or_b32 v1, s33, 12, v1
	s_waitcnt vmcnt(6)
	v_or_b32_e32 v3, v2, v0
	v_or_b32_e32 v198, v1, v0
	v_bitop3_b32 v2, v2, 64, v0 bitop3:0x36
	v_bitop3_b32 v199, v1, 64, v0 bitop3:0x36
	v_mov_b32_e32 v64, 0
	s_add_i32 s0, 0, 0x10000
	s_add_i32 s1, 0, 0x14000
	s_add_i32 s42, s7, 0xc000
	s_add_i32 s43, s7, 0xe000
	s_mov_b32 s44, -2
	s_mov_b64 s[10:11], 0
	v_add_u32_e32 v200, 0, v3
	v_add_u32_e32 v201, 0, v2
	s_add_i32 s45, 0, 0x18000
	v_mov_b32_e32 v65, v64
	v_mov_b32_e32 v66, v64
	v_mov_b32_e32 v67, v64
	v_mov_b32_e32 v68, v64
	v_mov_b32_e32 v69, v64
	v_mov_b32_e32 v70, v64
	v_mov_b32_e32 v71, v64
	v_mov_b32_e32 v80, v64
	v_mov_b32_e32 v81, v64
	v_mov_b32_e32 v82, v64
	v_mov_b32_e32 v83, v64
	v_mov_b32_e32 v84, v64
	v_mov_b32_e32 v85, v64
	v_mov_b32_e32 v86, v64
	v_mov_b32_e32 v87, v64
	v_mov_b32_e32 v96, v64
	v_mov_b32_e32 v97, v64
	v_mov_b32_e32 v98, v64
	v_mov_b32_e32 v99, v64
	v_mov_b32_e32 v100, v64
	v_mov_b32_e32 v101, v64
	v_mov_b32_e32 v102, v64
	v_mov_b32_e32 v103, v64
	v_mov_b32_e32 v112, v64
	v_mov_b32_e32 v113, v64
	v_mov_b32_e32 v114, v64
	v_mov_b32_e32 v115, v64
	v_mov_b32_e32 v116, v64
	v_mov_b32_e32 v117, v64
	v_mov_b32_e32 v118, v64
	v_mov_b32_e32 v119, v64
	v_mov_b32_e32 v72, v64
	v_mov_b32_e32 v73, v64
	v_mov_b32_e32 v74, v64
	v_mov_b32_e32 v75, v64
	v_mov_b32_e32 v76, v64
	v_mov_b32_e32 v77, v64
	v_mov_b32_e32 v78, v64
	v_mov_b32_e32 v79, v64
	v_mov_b32_e32 v88, v64
	v_mov_b32_e32 v89, v64
	v_mov_b32_e32 v90, v64
	v_mov_b32_e32 v91, v64
	v_mov_b32_e32 v92, v64
	v_mov_b32_e32 v93, v64
	v_mov_b32_e32 v94, v64
	v_mov_b32_e32 v95, v64
	v_mov_b32_e32 v104, v64
	v_mov_b32_e32 v105, v64
	v_mov_b32_e32 v106, v64
	v_mov_b32_e32 v107, v64
	v_mov_b32_e32 v108, v64
	v_mov_b32_e32 v109, v64
	v_mov_b32_e32 v110, v64
	v_mov_b32_e32 v111, v64
	v_mov_b32_e32 v120, v64
	v_mov_b32_e32 v121, v64
	v_mov_b32_e32 v122, v64
	v_mov_b32_e32 v123, v64
	v_mov_b32_e32 v124, v64
	v_mov_b32_e32 v125, v64
	v_mov_b32_e32 v126, v64
	v_mov_b32_e32 v127, v64
	v_mov_b32_e32 v128, v64
	v_mov_b32_e32 v129, v64
	v_mov_b32_e32 v130, v64
	v_mov_b32_e32 v131, v64
	v_mov_b32_e32 v132, v64
	v_mov_b32_e32 v133, v64
	v_mov_b32_e32 v134, v64
	v_mov_b32_e32 v135, v64
	v_mov_b32_e32 v144, v64
	v_mov_b32_e32 v145, v64
	v_mov_b32_e32 v146, v64
	v_mov_b32_e32 v147, v64
	v_mov_b32_e32 v148, v64
	v_mov_b32_e32 v149, v64
	v_mov_b32_e32 v150, v64
	v_mov_b32_e32 v151, v64
	v_mov_b32_e32 v160, v64
	v_mov_b32_e32 v161, v64
	v_mov_b32_e32 v162, v64
	v_mov_b32_e32 v163, v64
	v_mov_b32_e32 v164, v64
	v_mov_b32_e32 v165, v64
	v_mov_b32_e32 v166, v64
	v_mov_b32_e32 v167, v64
	v_mov_b32_e32 v176, v64
	v_mov_b32_e32 v177, v64
	v_mov_b32_e32 v178, v64
	v_mov_b32_e32 v179, v64
	v_mov_b32_e32 v180, v64
	v_mov_b32_e32 v181, v64
	v_mov_b32_e32 v182, v64
	v_mov_b32_e32 v183, v64
	v_mov_b32_e32 v136, v64
	v_mov_b32_e32 v137, v64
	v_mov_b32_e32 v138, v64
	v_mov_b32_e32 v139, v64
	v_mov_b32_e32 v140, v64
	v_mov_b32_e32 v141, v64
	v_mov_b32_e32 v142, v64
	v_mov_b32_e32 v143, v64
	v_mov_b32_e32 v152, v64
	v_mov_b32_e32 v153, v64
	v_mov_b32_e32 v154, v64
	v_mov_b32_e32 v155, v64
	v_mov_b32_e32 v156, v64
	v_mov_b32_e32 v157, v64
	v_mov_b32_e32 v158, v64
	v_mov_b32_e32 v159, v64
	v_mov_b32_e32 v168, v64
	v_mov_b32_e32 v169, v64
	v_mov_b32_e32 v170, v64
	v_mov_b32_e32 v171, v64
	v_mov_b32_e32 v172, v64
	v_mov_b32_e32 v173, v64
	v_mov_b32_e32 v174, v64
	v_mov_b32_e32 v175, v64
	v_mov_b32_e32 v184, v64
	v_mov_b32_e32 v185, v64
	v_mov_b32_e32 v186, v64
	v_mov_b32_e32 v187, v64
	v_mov_b32_e32 v188, v64
	v_mov_b32_e32 v189, v64
	v_mov_b32_e32 v190, v64
	v_mov_b32_e32 v191, v64
	v_add_u32_e32 v202, s0, v198
	v_add_u32_e32 v203, s0, v199
	v_add_u32_e32 v204, s1, v198
	v_add_u32_e32 v205, s1, v199
	s_barrier
	s_cmpk_eq_i32 s10, 0x700
	s_cselect_b64 s[18:19], -1, 0
	s_cmpk_lg_i32 s10, 0x700
	s_cselect_b64 s[24:25], -1, 0
	s_add_u32 s49, s16, s10
	s_addc_u32 s50, s9, s11
	s_add_u32 s46, s8, s10
	s_addc_u32 s47, s3, s11
	s_add_u32 s20, s46, 0x100
	s_addc_u32 s48, s47, 0
	s_add_u32 s12, s49, 0x40080
	s_addc_u32 s0, s50, 0
	s_and_b32 s13, s0, 0xffff
	v_add_u32_e32 v207, 0x18000, v198
	v_add_u32_e32 v208, 0x18000, v199
	v_add_u32_e32 v209, 0x1c000, v198
	v_add_u32_e32 v210, 0x1c000, v199
	s_mov_b32 s62, s14
	s_mov_b32 s63, s15
	s_mov_b32 s66, s14
	s_mov_b32 s67, s15
.Lp3_loop:
	ds_read_b128 v[0:3], v202
	ds_read_b128 v[8:11], v202 offset:2048
	ds_read_b128 v[4:7], v203
	ds_read_b128 v[12:15], v203 offset:2048
	ds_read_b128 v[24:27], v204
	ds_read_b128 v[16:19], v204 offset:2048
	ds_read_b128 v[28:31], v205
	ds_read_b128 v[20:23], v205 offset:2048
	ds_read_b128 v[56:59], v200
	ds_read_b128 v[48:51], v200 offset:2048
	ds_read_b128 v[60:63], v201
	ds_read_b128 v[52:55], v201 offset:2048
	ds_read_b128 v[40:43], v200 offset:4096
	ds_read_b128 v[32:35], v200 offset:6144
	ds_read_b128 v[44:47], v201 offset:4096
	ds_read_b128 v[36:39], v201 offset:6144
	s_add_u32 s60, s16, s10
	s_addc_u32 s61, s9, s11
	s_add_u32 s60, s60, 0x80
	s_addc_u32 s61, s61, 0
	s_and_b32 s61, s61, 0xffff
	s_mov_b32 m0, s38
	s_nop 0
	buffer_load_dwordx4 v192, s[60:63], 0 offen lds
	s_mov_b32 m0, s39
	s_nop 0
	buffer_load_dwordx4 v194, s[60:63], 0 offen lds
	s_add_u32 s60, s60, 0x40000
	s_addc_u32 s61, s61, 0
	s_mov_b32 m0, s42
	s_nop 0
	buffer_load_dwordx4 v192, s[60:63], 0 offen lds
	s_mov_b32 m0, s43
	s_nop 0
	buffer_load_dwordx4 v194, s[60:63], 0 offen lds
	s_waitcnt vmcnt(8) lgkmcnt(8)
	s_barrier
	s_waitcnt lgkmcnt(0)
	s_setprio 1
	v_mfma_f32_16x16x128_f8f6f4 v[188:191], v[0:7], v[56:63], v[188:191]
	v_mfma_f32_16x16x128_f8f6f4 v[184:187], v[8:15], v[56:63], v[184:187]
	v_mfma_f32_16x16x128_f8f6f4 v[172:175], v[0:7], v[48:55], v[172:175]
	v_mfma_f32_16x16x128_f8f6f4 v[168:171], v[8:15], v[48:55], v[168:171]
	v_mfma_f32_16x16x128_f8f6f4 v[156:159], v[0:7], v[40:47], v[156:159]
	v_mfma_f32_16x16x128_f8f6f4 v[152:155], v[8:15], v[40:47], v[152:155]
	v_mfma_f32_16x16x128_f8f6f4 v[140:143], v[0:7], v[32:39], v[140:143]
	v_mfma_f32_16x16x128_f8f6f4 v[136:139], v[8:15], v[32:39], v[136:139]
	v_mfma_f32_16x16x128_f8f6f4 v[180:183], v[24:31], v[56:63], v[180:183]
	v_mfma_f32_16x16x128_f8f6f4 v[176:179], v[16:23], v[56:63], v[176:179]
	v_mfma_f32_16x16x128_f8f6f4 v[164:167], v[24:31], v[48:55], v[164:167]
	v_mfma_f32_16x16x128_f8f6f4 v[160:163], v[16:23], v[48:55], v[160:163]
	v_mfma_f32_16x16x128_f8f6f4 v[148:151], v[24:31], v[40:47], v[148:151]
	v_mfma_f32_16x16x128_f8f6f4 v[144:147], v[16:23], v[40:47], v[144:147]
	v_mfma_f32_16x16x128_f8f6f4 v[132:135], v[24:31], v[32:39], v[132:135]
	v_mfma_f32_16x16x128_f8f6f4 v[128:131], v[16:23], v[32:39], v[128:131]
	s_setprio 0
	s_barrier
	ds_read_b128 v[56:59], v200 offset:16384
	ds_read_b128 v[48:51], v200 offset:18432
	ds_read_b128 v[60:63], v201 offset:16384
	ds_read_b128 v[52:55], v201 offset:18432
	ds_read_b128 v[40:43], v200 offset:20480
	ds_read_b128 v[32:35], v200 offset:22528
	ds_read_b128 v[44:47], v201 offset:20480
	ds_read_b128 v[36:39], v201 offset:22528
	s_waitcnt vmcnt(2)
	s_cmpk_eq_i32 s10, 0x700
	s_cbranch_scc1 .Lp3_b_skip
	s_add_u32 s64, s8, s10
	s_addc_u32 s65, s3, s11
	s_add_u32 s64, s64, 0x100
	s_addc_u32 s65, s65, 0
	s_and_b32 s65, s65, 0xffff
	s_mov_b32 m0, s28
	s_nop 0
	buffer_load_dwordx4 v193, s[64:67], 0 offen lds
	s_mov_b32 m0, s29
	s_nop 0
	buffer_load_dwordx4 v195, s[64:67], 0 offen lds
	s_add_u32 s64, s64, 0x4000
	s_addc_u32 s65, s65, 0
	s_mov_b32 m0, s17
	s_nop 0
	buffer_load_dwordx4 v193, s[64:67], 0 offen lds
	s_mov_b32 m0, s31
	s_nop 0
	buffer_load_dwordx4 v195, s[64:67], 0 offen lds
.Lp3_b_skip:
	s_waitcnt lgkmcnt(0)
	s_barrier
	s_setprio 1
	v_mfma_f32_16x16x128_f8f6f4 v[124:127], v[0:7], v[56:63], v[124:127]
	v_mfma_f32_16x16x128_f8f6f4 v[120:123], v[8:15], v[56:63], v[120:123]
	v_mfma_f32_16x16x128_f8f6f4 v[108:111], v[0:7], v[48:55], v[108:111]
	v_mfma_f32_16x16x128_f8f6f4 v[104:107], v[8:15], v[48:55], v[104:107]
	v_mfma_f32_16x16x128_f8f6f4 v[92:95], v[0:7], v[40:47], v[92:95]
	v_mfma_f32_16x16x128_f8f6f4 v[88:91], v[8:15], v[40:47], v[88:91]
	v_mfma_f32_16x16x128_f8f6f4 v[76:79], v[0:7], v[32:39], v[76:79]
	v_mfma_f32_16x16x128_f8f6f4 v[72:75], v[8:15], v[32:39], v[72:75]
	v_mfma_f32_16x16x128_f8f6f4 v[116:119], v[24:31], v[56:63], v[116:119]
	v_mfma_f32_16x16x128_f8f6f4 v[112:115], v[16:23], v[56:63], v[112:115]
	v_mfma_f32_16x16x128_f8f6f4 v[100:103], v[24:31], v[48:55], v[100:103]
	v_mfma_f32_16x16x128_f8f6f4 v[96:99], v[16:23], v[48:55], v[96:99]
	v_mfma_f32_16x16x128_f8f6f4 v[84:87], v[24:31], v[40:47], v[84:87]
	v_mfma_f32_16x16x128_f8f6f4 v[80:83], v[16:23], v[40:47], v[80:83]
	v_mfma_f32_16x16x128_f8f6f4 v[68:71], v[24:31], v[32:39], v[68:71]
	v_mfma_f32_16x16x128_f8f6f4 v[64:67], v[16:23], v[32:39], v[64:67]
	s_setprio 0
	s_barrier
	ds_read_b128 v[8:11], v207
	ds_read_b128 v[0:3], v207 offset:2048
	ds_read_b128 v[12:15], v208
	ds_read_b128 v[4:7], v208 offset:2048
	ds_read_b128 v[24:27], v209
	ds_read_b128 v[16:19], v209 offset:2048
	ds_read_b128 v[28:31], v210
	ds_read_b128 v[20:23], v210 offset:2048
	ds_read_b128 v[56:59], v200 offset:32768
	ds_read_b128 v[48:51], v200 offset:34816
	ds_read_b128 v[60:63], v201 offset:32768
	ds_read_b128 v[52:55], v201 offset:34816
	ds_read_b128 v[40:43], v200 offset:36864
	ds_read_b128 v[32:35], v200 offset:38912
	ds_read_b128 v[44:47], v201 offset:36864
	ds_read_b128 v[36:39], v201 offset:38912
	s_cmpk_eq_i32 s10, 0x700
	s_cbranch_scc1 .Lp3_c_fin
	s_add_u32 s60, s16, s10
	s_addc_u32 s61, s9, s11
	s_add_u32 s60, s60, 0x100
	s_addc_u32 s61, s61, 0
	s_and_b32 s61, s61, 0xffff
	s_mov_b32 m0, s7
	s_nop 0
	buffer_load_dwordx4 v192, s[60:63], 0 offen lds
	s_mov_b32 m0, s30
	s_nop 0
	buffer_load_dwordx4 v194, s[60:63], 0 offen lds
	s_add_u32 s60, s60, 0x40000
	s_addc_u32 s61, s61, 0
	s_mov_b32 m0, s34
	s_nop 0
	buffer_load_dwordx4 v192, s[60:63], 0 offen lds
	s_mov_b32 m0, s35
	s_nop 0
	buffer_load_dwordx4 v194, s[60:63], 0 offen lds
	s_waitcnt vmcnt(8)
	s_branch .Lp3_c_join

.Lp3_c_join:
	s_waitcnt lgkmcnt(8)
	s_barrier
	s_waitcnt lgkmcnt(0)
	s_setprio 1
	v_mfma_f32_16x16x128_f8f6f4 v[188:191], v[8:15], v[56:63], v[188:191]
	v_mfma_f32_16x16x128_f8f6f4 v[184:187], v[0:7], v[56:63], v[184:187]
	v_mfma_f32_16x16x128_f8f6f4 v[172:175], v[8:15], v[48:55], v[172:175]
	v_mfma_f32_16x16x128_f8f6f4 v[168:171], v[0:7], v[48:55], v[168:171]
	v_mfma_f32_16x16x128_f8f6f4 v[156:159], v[8:15], v[40:47], v[156:159]
	v_mfma_f32_16x16x128_f8f6f4 v[152:155], v[0:7], v[40:47], v[152:155]
	v_mfma_f32_16x16x128_f8f6f4 v[140:143], v[8:15], v[32:39], v[140:143]
	v_mfma_f32_16x16x128_f8f6f4 v[136:139], v[0:7], v[32:39], v[136:139]
	v_mfma_f32_16x16x128_f8f6f4 v[180:183], v[24:31], v[56:63], v[180:183]
	v_mfma_f32_16x16x128_f8f6f4 v[176:179], v[16:23], v[56:63], v[176:179]
	v_mfma_f32_16x16x128_f8f6f4 v[164:167], v[24:31], v[48:55], v[164:167]
	v_mfma_f32_16x16x128_f8f6f4 v[160:163], v[16:23], v[48:55], v[160:163]
	v_mfma_f32_16x16x128_f8f6f4 v[148:151], v[24:31], v[40:47], v[148:151]
	v_mfma_f32_16x16x128_f8f6f4 v[144:147], v[16:23], v[40:47], v[144:147]
	v_mfma_f32_16x16x128_f8f6f4 v[132:135], v[24:31], v[32:39], v[132:135]
	v_mfma_f32_16x16x128_f8f6f4 v[128:131], v[16:23], v[32:39], v[128:131]
	s_setprio 0
	s_barrier
	ds_read_b128 v[56:59], v200 offset:49152
	ds_read_b128 v[48:51], v200 offset:51200
	ds_read_b128 v[60:63], v201 offset:49152
	ds_read_b128 v[52:55], v201 offset:51200
	ds_read_b128 v[40:43], v200 offset:53248
	ds_read_b128 v[32:35], v200 offset:55296
	ds_read_b128 v[44:47], v201 offset:53248
	ds_read_b128 v[36:39], v201 offset:55296
	s_cmpk_eq_i32 s10, 0x700
	s_cbranch_scc1 .Lp3_d_skip
	s_add_u32 s64, s8, s10
	s_addc_u32 s65, s3, s11
	s_add_u32 s64, s64, 0x180
	s_addc_u32 s65, s65, 0
	s_and_b32 s65, s65, 0xffff
	s_mov_b32 m0, s36
	s_nop 0
	buffer_load_dwordx4 v193, s[64:67], 0 offen lds
	s_mov_b32 m0, s37
	s_nop 0
	buffer_load_dwordx4 v195, s[64:67], 0 offen lds
	s_add_u32 s64, s64, 0x4000
	s_addc_u32 s65, s65, 0
	s_mov_b32 m0, s40
	s_nop 0
	buffer_load_dwordx4 v193, s[64:67], 0 offen lds
	s_mov_b32 m0, s41
	s_nop 0
	buffer_load_dwordx4 v195, s[64:67], 0 offen lds
.Lp3_d_skip:
	s_waitcnt vmcnt(6) lgkmcnt(0)
	s_barrier
	s_setprio 1
	v_mfma_f32_16x16x128_f8f6f4 v[124:127], v[8:15], v[56:63], v[124:127]
	s_add_i32 s44, s44, 2
	s_add_u32 s10, s10, 0x100
	s_addc_u32 s11, s11, 0
	s_cmp_gt_u32 s44, 13
	v_mfma_f32_16x16x128_f8f6f4 v[120:123], v[0:7], v[56:63], v[120:123]
	v_mfma_f32_16x16x128_f8f6f4 v[108:111], v[8:15], v[48:55], v[108:111]
	v_mfma_f32_16x16x128_f8f6f4 v[104:107], v[0:7], v[48:55], v[104:107]
	v_mfma_f32_16x16x128_f8f6f4 v[92:95], v[8:15], v[40:47], v[92:95]
	v_mfma_f32_16x16x128_f8f6f4 v[88:91], v[0:7], v[40:47], v[88:91]
	v_mfma_f32_16x16x128_f8f6f4 v[76:79], v[8:15], v[32:39], v[76:79]
	v_mfma_f32_16x16x128_f8f6f4 v[72:75], v[0:7], v[32:39], v[72:75]
	v_mfma_f32_16x16x128_f8f6f4 v[116:119], v[24:31], v[56:63], v[116:119]
	v_mfma_f32_16x16x128_f8f6f4 v[112:115], v[16:23], v[56:63], v[112:115]
	v_mfma_f32_16x16x128_f8f6f4 v[100:103], v[24:31], v[48:55], v[100:103]
	v_mfma_f32_16x16x128_f8f6f4 v[96:99], v[16:23], v[48:55], v[96:99]
	v_mfma_f32_16x16x128_f8f6f4 v[84:87], v[24:31], v[40:47], v[84:87]
	v_mfma_f32_16x16x128_f8f6f4 v[80:83], v[16:23], v[40:47], v[80:83]
	v_mfma_f32_16x16x128_f8f6f4 v[68:71], v[24:31], v[32:39], v[68:71]
	v_mfma_f32_16x16x128_f8f6f4 v[64:67], v[16:23], v[32:39], v[64:67]
	s_setprio 0
	s_barrier
	s_cbranch_scc0 .Lp3_loop

	.amdhsa_kernel _ZN2rb6k_gemmILi1ENS_6SchedGILb1EEENS_5EpiP3EEEvT0_T1_
		.amdhsa_group_segment_fixed_size 0
		.amdhsa_private_segment_fixed_size 0
		.amdhsa_kernarg_size 48
		.amdhsa_user_sgpr_count 2
		.amdhsa_user_sgpr_dispatch_ptr 0
		.amdhsa_user_sgpr_queue_ptr 0
		.amdhsa_user_sgpr_kernarg_segment_ptr 1
		.amdhsa_user_sgpr_dispatch_id 0
		.amdhsa_user_sgpr_kernarg_preload_length 0
		.amdhsa_user_sgpr_kernarg_preload_offset 0
		.amdhsa_user_sgpr_private_segment_size 0
		.amdhsa_uses_dynamic_stack 0
		.amdhsa_enable_private_segment 0
		.amdhsa_system_sgpr_workgroup_id_x 1
		.amdhsa_system_sgpr_workgroup_id_y 0
		.amdhsa_system_sgpr_workgroup_id_z 0
		.amdhsa_system_sgpr_workgroup_info 0
		.amdhsa_system_vgpr_workitem_id 0
		.amdhsa_next_free_vgpr 211
		.amdhsa_next_free_sgpr 68
		.amdhsa_accum_offset 212
		.amdhsa_reserve_vcc 1
		.amdhsa_float_round_mode_32 0
		.amdhsa_float_round_mode_16_64 0
		.amdhsa_float_denorm_mode_32 3
		.amdhsa_float_denorm_mode_16_64 3
		.amdhsa_dx10_clamp 1
		.amdhsa_ieee_mode 1
		.amdhsa_fp16_overflow 0
		.amdhsa_tg_split 0
		.amdhsa_exception_fp_ieee_invalid_op 0
		.amdhsa_exception_fp_denorm_src 0
		.amdhsa_exception_fp_ieee_div_zero 0
		.amdhsa_exception_fp_ieee_overflow 0
		.amdhsa_exception_fp_ieee_underflow 0
		.amdhsa_exception_fp_ieee_inexact 0
		.amdhsa_exception_int_div_zero 0
	.end_amdhsa_kernel

amdhsa.kernels:
  - .agpr_count:     0
    .args:
      - .actual_access:  read_only
        .address_space:  global
        .offset:         0
        .size:           8
        .value_kind:     global_buffer
      - .actual_access:  read_only
        .address_space:  global
        .offset:         8
        .size:           8
        .value_kind:     global_buffer
      - .actual_access:  read_only
        .address_space:  global
        .offset:         16
        .size:           8
        .value_kind:     global_buffer
      - .actual_access:  read_only
        .address_space:  global
        .offset:         24
        .size:           8
        .value_kind:     global_buffer
      - .actual_access:  read_only
        .address_space:  global
        .offset:         32
        .size:           8
        .value_kind:     global_buffer
      - .actual_access:  read_only
        .address_space:  global
        .offset:         40
        .size:           8
        .value_kind:     global_buffer
      - .actual_access:  read_only
        .address_space:  global
        .offset:         48
        .size:           8
        .value_kind:     global_buffer
      - .actual_access:  read_only
        .address_space:  global
        .offset:         56
        .size:           8
        .value_kind:     global_buffer
      - .actual_access:  write_only
        .address_space:  global
        .offset:         64
        .size:           8
        .value_kind:     global_buffer
      - .offset:         72
        .size:           4
        .value_kind:     by_value
    .group_segment_fixed_size: 32768
    .kernarg_segment_align: 8
    .kernarg_segment_size: 76
    .language:       OpenCL C
    .language_version:
      - 2
      - 0
    .max_flat_workgroup_size: 256
    .name:           _ZN2rb6k_prepEPKfS1_S1_S1_S1_S1_S1_S1_Phi
    .private_segment_fixed_size: 0
    .sgpr_count:     22
    .sgpr_spill_count: 0
    .symbol:         _ZN2rb6k_prepEPKfS1_S1_S1_S1_S1_S1_S1_Phi.kd
    .uniform_work_group_size: 1
    .uses_dynamic_stack: false
    .vgpr_count:     100
    .vgpr_spill_count: 0
    .wavefront_size: 64
  - .agpr_count:     0
    .args:
      - .address_space:  global
        .offset:         0
        .size:           8
        .value_kind:     global_buffer
      - .actual_access:  read_only
        .address_space:  global
        .offset:         8
        .size:           8
        .value_kind:     global_buffer
    .group_segment_fixed_size: 0
    .kernarg_segment_align: 8
    .kernarg_segment_size: 16
    .language:       OpenCL C
    .language_version:
      - 2
      - 0
    .max_flat_workgroup_size: 256
    .name:           _ZN2rb5k_midEPhPKf
    .private_segment_fixed_size: 0
    .sgpr_count:     20
    .sgpr_spill_count: 0
    .symbol:         _ZN2rb5k_midEPhPKf.kd
    .uniform_work_group_size: 1
    .uses_dynamic_stack: false
    .vgpr_count:     86
    .vgpr_spill_count: 0
    .wavefront_size: 64
  - .agpr_count:     0
    .args:
      - .offset:         0
        .size:           24
        .value_kind:     by_value
      - .offset:         24
        .size:           64
        .value_kind:     by_value
    .group_segment_fixed_size: 0
    .kernarg_segment_align: 8
    .kernarg_segment_size: 88
    .language:       OpenCL C
    .language_version:
      - 2
      - 0
    .max_flat_workgroup_size: 512
    .name:           _ZN2rb6k_gemmILi2ENS_7SchedP1ENS_5EpiP1EEEvT0_T1_
    .private_segment_fixed_size: 0
    .sgpr_count:     86
    .sgpr_spill_count: 0
    .symbol:         _ZN2rb6k_gemmILi2ENS_7SchedP1ENS_5EpiP1EEEvT0_T1_.kd
    .uniform_work_group_size: 1
    .uses_dynamic_stack: false
    .vgpr_count:     212
    .vgpr_spill_count: 0
    .wavefront_size: 64
  - .agpr_count:     0
    .args:
      - .offset:         0
        .size:           24
        .value_kind:     by_value
      - .offset:         24
        .size:           16
        .value_kind:     by_value
    .group_segment_fixed_size: 0
    .kernarg_segment_align: 8
    .kernarg_segment_size: 40
    .language:       OpenCL C
    .language_version:
      - 2
      - 0
    .max_flat_workgroup_size: 512
    .name:           _ZN2rb6k_gemmILi1ENS_7SchedP2ENS_7EpiSlabEEEvT0_T1_
    .private_segment_fixed_size: 0
    .sgpr_count:     73
    .sgpr_spill_count: 0
    .symbol:         _ZN2rb6k_gemmILi1ENS_7SchedP2ENS_7EpiSlabEEEvT0_T1_.kd
    .uniform_work_group_size: 1
    .uses_dynamic_stack: false
    .vgpr_count:     210
    .vgpr_spill_count: 0
    .wavefront_size: 64
  - .agpr_count:     0
    .args:
      - .offset:         0
        .size:           32
        .value_kind:     by_value
      - .offset:         32
        .size:           16
        .value_kind:     by_value
    .group_segment_fixed_size: 0
    .kernarg_segment_align: 8
    .kernarg_segment_size: 48
    .language:       OpenCL C
    .language_version:
      - 2
      - 0
    .max_flat_workgroup_size: 512
    .name:           _ZN2rb6k_gemmILi1ENS_6SchedGILb1EEENS_5EpiP3EEEvT0_T1_
    .private_segment_fixed_size: 0
    .sgpr_count:     74
    .sgpr_spill_count: 0
    .symbol:         _ZN2rb6k_gemmILi1ENS_6SchedGILb1EEENS_5EpiP3EEEvT0_T1_.kd
    .uniform_work_group_size: 1
    .uses_dynamic_stack: false
    .vgpr_count:     211
    .vgpr_spill_count: 0
    .wavefront_size: 64
  - .agpr_count:     0
    .args:
      - .offset:         0
        .size:           32
        .value_kind:     by_value
      - .offset:         32
        .size:           48
        .value_kind:     by_value
    .group_segment_fixed_size: 0
    .kernarg_segment_align: 8
    .kernarg_segment_size: 80
    .language:       OpenCL C
    .language_version:
      - 2
      - 0
    .max_flat_workgroup_size: 512
    .name:           _ZN2rb6k_gemmILi1ENS_6SchedGILb1EEENS_6EpiOutEEEvT0_T1_
    .private_segment_fixed_size: 0
    .sgpr_count:     62
    .sgpr_spill_count: 0
    .symbol:         _ZN2rb6k_gemmILi1ENS_6SchedGILb1EEENS_6EpiOutEEEvT0_T1_.kd
    .uniform_work_group_size: 1
    .uses_dynamic_stack: false
    .vgpr_count:     205
    .vgpr_spill_count: 0
    .wavefront_size: 64
  - .agpr_count:     0
    .args:
      - .offset:         0
        .size:           24
        .value_kind:     by_value
      - .offset:         24
        .size:           1
        .value_kind:     by_value
    .group_segment_fixed_size: 0
    .kernarg_segment_align: 8
    .kernarg_segment_size: 28
    .language:       OpenCL C
    .language_version:
      - 2
      - 0
    .max_flat_workgroup_size: 512
    .name:           _ZN2rb6k_gemmILi2ENS_7SchedP1ENS_7EpiNullEEEvT0_T1_
    .private_segment_fixed_size: 0
    .sgpr_count:     66
    .sgpr_spill_count: 0
    .symbol:         _ZN2rb6k_gemmILi2ENS_7SchedP1ENS_7EpiNullEEEvT0_T1_.kd
    .uniform_work_group_size: 1
    .uses_dynamic_stack: false
    .vgpr_count:     205
    .vgpr_spill_count: 0
    .wavefront_size: 64
